# speedup vs baseline: 1.0160x; 1.0062x over previous
.Lg0_cloop:
	s_mul_i32 s8, s3, 0x7000
	s_barrier
	v_add_u32_e32 v103, s8, v100
	v_add_u32_e32 v101, s8, v99
	ds_read_b128 v[146:149], v103 offset:12288
	ds_read_b128 v[150:153], v103 offset:13312
	ds_read_b128 v[154:157], v103 offset:14336
	ds_read_b128 v[158:161], v103 offset:15360
	s_waitcnt lgkmcnt(9)
	v_mfma_f32_16x16x32_f16 v[94:97], v[122:125], v[104:107], v[94:97]
	s_add_i32 s8, s3, 1
	s_cmp_lg_u32 s3, 4
	s_cselect_b32 s3, s8, 0
	v_mfma_f32_16x16x32_f16 v[70:73], v[122:125], v[108:111], v[70:73]
	v_mfma_f32_16x16x32_f16 v[46:49], v[122:125], v[112:115], v[46:49]
	v_mfma_f32_16x16x32_f16 v[22:25], v[122:125], v[116:119], v[22:25]
	ds_read_b128 v[122:125], v101
	s_waitcnt lgkmcnt(9)
	v_mfma_f32_16x16x32_f16 v[90:93], v[126:129], v[104:107], v[90:93]
	v_mfma_f32_16x16x32_f16 v[66:69], v[126:129], v[108:111], v[66:69]
	v_mfma_f32_16x16x32_f16 v[42:45], v[126:129], v[112:115], v[42:45]
	v_mfma_f32_16x16x32_f16 v[18:21], v[126:129], v[116:119], v[18:21]
	ds_read_b128 v[126:129], v101 offset:1024
	s_waitcnt lgkmcnt(9)
	v_mfma_f32_16x16x32_f16 v[86:89], v[130:133], v[104:107], v[86:89]
	v_mfma_f32_16x16x32_f16 v[54:57], v[130:133], v[108:111], v[54:57]
	v_mfma_f32_16x16x32_f16 v[26:29], v[130:133], v[112:115], v[26:29]
	v_mfma_f32_16x16x32_f16 v[6:9], v[130:133], v[116:119], v[6:9]
	ds_read_b128 v[130:133], v101 offset:2048
	s_waitcnt lgkmcnt(9)
	v_mfma_f32_16x16x32_f16 v[74:77], v[134:137], v[104:107], v[74:77]
	v_mfma_f32_16x16x32_f16 v[50:53], v[134:137], v[108:111], v[50:53]
	v_mfma_f32_16x16x32_f16 v[38:41], v[134:137], v[112:115], v[38:41]
	v_mfma_f32_16x16x32_f16 v[14:17], v[134:137], v[116:119], v[14:17]
	ds_read_b128 v[134:137], v101 offset:3072
	s_waitcnt lgkmcnt(9)
	v_mfma_f32_16x16x32_f16 v[82:85], v[138:141], v[104:107], v[82:85]
	v_mfma_f32_16x16x32_f16 v[58:61], v[138:141], v[108:111], v[58:61]
	v_mfma_f32_16x16x32_f16 v[30:33], v[138:141], v[112:115], v[30:33]
	v_mfma_f32_16x16x32_f16 v[10:13], v[138:141], v[116:119], v[10:13]
	ds_read_b128 v[138:141], v101 offset:4096
	s_waitcnt lgkmcnt(9)
	v_mfma_f32_16x16x32_f16 v[78:81], v[142:145], v[104:107], v[78:81]
	v_mfma_f32_16x16x32_f16 v[62:65], v[142:145], v[108:111], v[62:65]
	v_mfma_f32_16x16x32_f16 v[34:37], v[142:145], v[112:115], v[34:37]
	v_mfma_f32_16x16x32_f16 v[2:5], v[142:145], v[116:119], v[2:5]
	ds_read_b128 v[142:145], v101 offset:5120
	s_mul_i32 s8, s3, 0x7000
	s_barrier
	v_add_u32_e32 v103, s8, v100
	v_add_u32_e32 v101, s8, v99
	ds_read_b128 v[104:107], v103 offset:12288
	ds_read_b128 v[108:111], v103 offset:13312
	ds_read_b128 v[112:115], v103 offset:14336
	ds_read_b128 v[116:119], v103 offset:15360
	s_waitcnt lgkmcnt(9)
	v_mfma_f32_16x16x32_f16 v[94:97], v[122:125], v[146:149], v[94:97]
	s_add_i32 s8, s3, 1
	s_cmp_lg_u32 s3, 4
	s_cselect_b32 s3, s8, 0
	v_mfma_f32_16x16x32_f16 v[70:73], v[122:125], v[150:153], v[70:73]
	v_mfma_f32_16x16x32_f16 v[46:49], v[122:125], v[154:157], v[46:49]
	v_mfma_f32_16x16x32_f16 v[22:25], v[122:125], v[158:161], v[22:25]
	ds_read_b128 v[122:125], v101
	s_waitcnt lgkmcnt(9)
	v_mfma_f32_16x16x32_f16 v[90:93], v[126:129], v[146:149], v[90:93]
	v_mfma_f32_16x16x32_f16 v[66:69], v[126:129], v[150:153], v[66:69]
	v_mfma_f32_16x16x32_f16 v[42:45], v[126:129], v[154:157], v[42:45]
	v_mfma_f32_16x16x32_f16 v[18:21], v[126:129], v[158:161], v[18:21]
	ds_read_b128 v[126:129], v101 offset:1024
	s_waitcnt lgkmcnt(9)
	v_mfma_f32_16x16x32_f16 v[86:89], v[130:133], v[146:149], v[86:89]
	v_mfma_f32_16x16x32_f16 v[54:57], v[130:133], v[150:153], v[54:57]
	v_mfma_f32_16x16x32_f16 v[26:29], v[130:133], v[154:157], v[26:29]
	v_mfma_f32_16x16x32_f16 v[6:9], v[130:133], v[158:161], v[6:9]
	ds_read_b128 v[130:133], v101 offset:2048
	s_waitcnt lgkmcnt(9)
	v_mfma_f32_16x16x32_f16 v[74:77], v[134:137], v[146:149], v[74:77]
	v_mfma_f32_16x16x32_f16 v[50:53], v[134:137], v[150:153], v[50:53]
	v_mfma_f32_16x16x32_f16 v[38:41], v[134:137], v[154:157], v[38:41]
	v_mfma_f32_16x16x32_f16 v[14:17], v[134:137], v[158:161], v[14:17]
	ds_read_b128 v[134:137], v101 offset:3072
	s_waitcnt lgkmcnt(9)
	v_mfma_f32_16x16x32_f16 v[82:85], v[138:141], v[146:149], v[82:85]
	v_mfma_f32_16x16x32_f16 v[58:61], v[138:141], v[150:153], v[58:61]
	v_mfma_f32_16x16x32_f16 v[30:33], v[138:141], v[154:157], v[30:33]
	v_mfma_f32_16x16x32_f16 v[10:13], v[138:141], v[158:161], v[10:13]
	ds_read_b128 v[138:141], v101 offset:4096
	s_waitcnt lgkmcnt(9)
	v_mfma_f32_16x16x32_f16 v[78:81], v[142:145], v[146:149], v[78:81]
	v_mfma_f32_16x16x32_f16 v[62:65], v[142:145], v[150:153], v[62:65]
	v_mfma_f32_16x16x32_f16 v[34:37], v[142:145], v[154:157], v[34:37]
	v_mfma_f32_16x16x32_f16 v[2:5], v[142:145], v[158:161], v[2:5]
	ds_read_b128 v[142:145], v101 offset:5120
	s_add_i32 s7, s7, -1
	s_cmp_eq_u32 s7, 0
	s_cbranch_scc0 .Lg0_cloop
	s_waitcnt lgkmcnt(0)
	s_barrier
	s_mul_i32 s24, s22, 0x3400
	s_lshl_b32 s28, s2, 6
	s_add_i32 s29, s20, s28
	s_and_b32 s30, s29, 0x7ff
	v_add_u32_e32 v98, s30, v102
	v_lshlrev_b32_e32 v98, 8, v98
	v_lshl_add_u32 v98, v120, 4, v98
	v_add_u32_e32 v99, 0x1000, v98
	v_add_u32_e32 v100, 0x2000, v98
	v_add_u32_e32 v101, 0x3000, v98
	v_mul_u32_u24_e32 v103, 0xd0, v102
	v_lshl_add_u32 v103, v120, 3, v103
	v_add_u32_e32 v103, s24, v103
	v_lshrrev_b32_e32 v0, 2, v1
	v_and_b32_e32 v1, 3, v1
	v_mul_u32_u24_e32 v102, 0xd0, v0
	v_lshl_add_u32 v102, v1, 4, v102
	v_add_u32_e32 v102, s24, v102
	v_lshlrev_b32_e32 v0, 11, v0
	v_lshl_add_u32 v0, v1, 4, v0
	s_lshl_b32 s31, s5, 7
	s_add_i32 s35, s31, 0
	s_and_b32 s35, s35, 0xff
	s_add_u32 s36, s12, s35
	s_addc_u32 s37, s13, 0
	s_add_i32 s35, s31, 64
	s_and_b32 s35, s35, 0xff
	s_add_u32 s38, s12, s35
	s_addc_u32 s39, s13, 0
	s_add_i32 s35, s31, 128
	s_and_b32 s35, s35, 0xff
	s_add_u32 s40, s12, s35
	s_addc_u32 s41, s13, 0
	s_add_i32 s35, s31, 192
	s_and_b32 s35, s35, 0xff
	s_add_u32 s42, s12, s35
	s_addc_u32 s43, s13, 0
	s_add_i32 s34, s25, s23
	s_sub_i32 s32, 0x400, s34
	s_ashr_i32 s32, s32, 4
	s_max_i32 s32, s32, 0
	s_min_i32 s32, s32, 6
	s_sub_i32 s33, 0x800, s34
	s_ashr_i32 s33, s33, 4
	s_max_i32 s33, s33, 0
	s_min_i32 s33, s33, 6
	s_cmp_eq_u32 s33, 0
	s_cbranch_scc1 .Lepi_noload
	global_load_dwordx4 v[104:107], v98, s[36:37]
	global_load_dwordx4 v[108:111], v98, s[38:39]
	global_load_dwordx4 v[112:115], v98, s[40:41]
	global_load_dwordx4 v[116:119], v98, s[42:43]
	global_load_dwordx4 v[120:123], v99, s[36:37]
	global_load_dwordx4 v[124:127], v99, s[38:39]
	global_load_dwordx4 v[128:131], v99, s[40:41]
	global_load_dwordx4 v[132:135], v99, s[42:43]
	global_load_dwordx4 v[136:139], v100, s[36:37]
	global_load_dwordx4 v[140:143], v100, s[38:39]
	global_load_dwordx4 v[144:147], v100, s[40:41]
	global_load_dwordx4 v[148:151], v100, s[42:43]
	global_load_dwordx4 v[152:155], v101, s[36:37]
	global_load_dwordx4 v[156:159], v101, s[38:39]
	global_load_dwordx4 v[160:163], v101, s[40:41]
	global_load_dwordx4 v[164:167], v101, s[42:43]
.Lepi_noload:
	s_cmp_le_u32 s33, 5
	s_cbranch_scc1 .Lepi_v5
	s_waitcnt vmcnt(0)
	s_cmp_lg_u32 s32, 6
	s_cbranch_scc1 .Lepi_r5
	v_mul_f32_e32 v104, 0x3e38aa3b, v104
	v_mul_f32_e32 v105, 0x3e38aa3b, v105
	v_mul_f32_e32 v106, 0x3e38aa3b, v106
	v_mul_f32_e32 v107, 0x3e38aa3b, v107
	v_mul_f32_e32 v108, 0x3e38aa3b, v108
	v_mul_f32_e32 v109, 0x3e38aa3b, v109
	v_mul_f32_e32 v110, 0x3e38aa3b, v110
	v_mul_f32_e32 v111, 0x3e38aa3b, v111
	v_mul_f32_e32 v112, 0x3e38aa3b, v112
	v_mul_f32_e32 v113, 0x3e38aa3b, v113
	v_mul_f32_e32 v114, 0x3e38aa3b, v114
	v_mul_f32_e32 v115, 0x3e38aa3b, v115
	v_mul_f32_e32 v116, 0x3e38aa3b, v116
	v_mul_f32_e32 v117, 0x3e38aa3b, v117
	v_mul_f32_e32 v118, 0x3e38aa3b, v118
	v_mul_f32_e32 v119, 0x3e38aa3b, v119
	v_mul_f32_e32 v120, 0x3e38aa3b, v120
	v_mul_f32_e32 v121, 0x3e38aa3b, v121
	v_mul_f32_e32 v122, 0x3e38aa3b, v122
	v_mul_f32_e32 v123, 0x3e38aa3b, v123
	v_mul_f32_e32 v124, 0x3e38aa3b, v124
	v_mul_f32_e32 v125, 0x3e38aa3b, v125
	v_mul_f32_e32 v126, 0x3e38aa3b, v126
	v_mul_f32_e32 v127, 0x3e38aa3b, v127
	v_mul_f32_e32 v128, 0x3e38aa3b, v128
	v_mul_f32_e32 v129, 0x3e38aa3b, v129
	v_mul_f32_e32 v130, 0x3e38aa3b, v130
	v_mul_f32_e32 v131, 0x3e38aa3b, v131
	v_mul_f32_e32 v132, 0x3e38aa3b, v132
	v_mul_f32_e32 v133, 0x3e38aa3b, v133
	v_mul_f32_e32 v134, 0x3e38aa3b, v134
	v_mul_f32_e32 v135, 0x3e38aa3b, v135
	v_mul_f32_e32 v136, 0x3e38aa3b, v136
	v_mul_f32_e32 v137, 0x3e38aa3b, v137
	v_mul_f32_e32 v138, 0x3e38aa3b, v138
	v_mul_f32_e32 v139, 0x3e38aa3b, v139
	v_mul_f32_e32 v140, 0x3e38aa3b, v140
	v_mul_f32_e32 v141, 0x3e38aa3b, v141
	v_mul_f32_e32 v142, 0x3e38aa3b, v142
	v_mul_f32_e32 v143, 0x3e38aa3b, v143
	v_mul_f32_e32 v144, 0x3e38aa3b, v144
	v_mul_f32_e32 v145, 0x3e38aa3b, v145
	v_mul_f32_e32 v146, 0x3e38aa3b, v146
	v_mul_f32_e32 v147, 0x3e38aa3b, v147
	v_mul_f32_e32 v148, 0x3e38aa3b, v148
	v_mul_f32_e32 v149, 0x3e38aa3b, v149
	v_mul_f32_e32 v150, 0x3e38aa3b, v150
	v_mul_f32_e32 v151, 0x3e38aa3b, v151
	v_mul_f32_e32 v152, 0x3e38aa3b, v152
	v_mul_f32_e32 v153, 0x3e38aa3b, v153
	v_mul_f32_e32 v154, 0x3e38aa3b, v154
	v_mul_f32_e32 v155, 0x3e38aa3b, v155
	v_mul_f32_e32 v156, 0x3e38aa3b, v156
	v_mul_f32_e32 v157, 0x3e38aa3b, v157
	v_mul_f32_e32 v158, 0x3e38aa3b, v158
	v_mul_f32_e32 v159, 0x3e38aa3b, v159
	v_mul_f32_e32 v160, 0x3e38aa3b, v160
	v_mul_f32_e32 v161, 0x3e38aa3b, v161
	v_mul_f32_e32 v162, 0x3e38aa3b, v162
	v_mul_f32_e32 v163, 0x3e38aa3b, v163
	v_mul_f32_e32 v164, 0x3e38aa3b, v164
	v_mul_f32_e32 v165, 0x3e38aa3b, v165
	v_mul_f32_e32 v166, 0x3e38aa3b, v166
	v_mul_f32_e32 v167, 0x3e38aa3b, v167
